# s7 + attention row-max: merged the x=max(x,x) canonicalisation no-ops (18 sites, -36 VALU)
# baseline (speedup 1.0000x reference)
.LBB0_479:
	v_add_f32_e32 v198, v235, v68
	v_max_f32_e32 v68, v49, v48
	v_max3_f32 v69, v50, v51, v33
	v_max3_f32 v68, v68, v32, v34
	v_max3_f32 v68, v68, v35, v52
	v_max3_f32 v69, v69, v54, v55
	v_max3_f32 v68, v68, v53, v36
	v_max3_f32 v69, v69, v38, v39
	v_max3_f32 v68, v68, v37, v56
	v_max3_f32 v69, v69, v58, v59
	v_max3_f32 v68, v68, v57, v40
	v_max3_f32 v69, v69, v42, v43
	v_max3_f32 v68, v68, v41, v60
	v_max3_f32 v69, v69, v62, v63
	v_max3_f32 v68, v68, v61, v44
	v_max3_f32 v69, v69, v46, v47
	v_max3_f32 v68, v68, v45, v69
	v_mov_b32_e32 v69, v68
	s_nop 1
	v_permlane32_swap_b32_e32 v68, v69
	v_max_f32_e32 v68, v69, v68
	v_cmp_lt_f32_e32 vcc, s49, v68
	s_cmp_lg_u64 vcc, 0
	s_cselect_b64 s[0:1], -1, 0
	s_cbranch_vccnz .LBB0_489

.LBB0_484:
	v_add_f32_e32 v235, v198, v36
	v_max_f32_e32 v36, v81, v80
	v_max3_f32 v37, v82, v83, v65
	v_max3_f32 v36, v36, v64, v66
	v_max3_f32 v36, v36, v67, v84
	v_max3_f32 v37, v37, v86, v87
	v_max3_f32 v36, v36, v85, v68
	v_max3_f32 v37, v37, v70, v71
	v_max3_f32 v36, v36, v69, v88
	v_max3_f32 v37, v37, v90, v91
	v_max3_f32 v36, v36, v89, v72
	v_max3_f32 v37, v37, v74, v75
	v_max3_f32 v36, v36, v73, v92
	v_max3_f32 v37, v37, v94, v95
	v_max3_f32 v36, v36, v93, v76
	v_max3_f32 v37, v37, v78, v79
	v_max3_f32 v36, v36, v77, v37
	v_mov_b32_e32 v37, v36
	s_nop 1
	v_permlane32_swap_b32_e32 v36, v37
	v_max_f32_e32 v36, v37, v36
	v_cmp_lt_f32_e32 vcc, s49, v36
	s_cmp_lg_u64 vcc, 0
	s_cselect_b64 s[40:41], -1, 0
	s_cbranch_vccnz .LBB0_492

.LBB0_502:
	v_add_f32_e32 v235, v235, v69
	v_max_f32_e32 v69, v49, v48
	v_max3_f32 v70, v50, v51, v33
	v_max3_f32 v69, v69, v32, v34
	v_max3_f32 v69, v69, v35, v52
	v_max3_f32 v70, v70, v54, v55
	v_max3_f32 v69, v69, v53, v36
	v_max3_f32 v70, v70, v38, v39
	v_max3_f32 v69, v69, v37, v56
	v_max3_f32 v70, v70, v58, v59
	v_max3_f32 v69, v69, v57, v40
	v_max3_f32 v70, v70, v42, v43
	v_max3_f32 v69, v69, v41, v60
	v_max3_f32 v70, v70, v62, v63
	v_max3_f32 v69, v69, v61, v44
	v_max3_f32 v70, v70, v46, v47
	v_max3_f32 v69, v69, v45, v70
	v_mov_b32_e32 v70, v69
	s_nop 1
	v_permlane32_swap_b32_e32 v69, v70
	v_max_f32_e32 v69, v70, v69
	v_cmp_lt_f32_e32 vcc, s49, v69
	s_cmp_lg_u64 vcc, 0
	s_cselect_b64 s[0:1], -1, 0
	s_cbranch_vccnz .LBB0_558

.LBB0_515:
	v_add_f32_e32 v235, v235, v239
	v_max_f32_e32 v239, v81, v80
	v_max3_f32 v240, v82, v83, v65
	v_max3_f32 v239, v239, v64, v66
	v_max3_f32 v239, v239, v67, v84
	v_max3_f32 v240, v240, v86, v87
	v_max3_f32 v239, v239, v85, v68
	v_max3_f32 v240, v240, v70, v71
	v_max3_f32 v239, v239, v69, v88
	v_max3_f32 v240, v240, v90, v91
	v_max3_f32 v239, v239, v89, v72
	v_max3_f32 v240, v240, v74, v75
	v_max3_f32 v239, v239, v73, v92
	v_max3_f32 v240, v240, v94, v95
	v_max3_f32 v239, v239, v93, v76
	v_max3_f32 v240, v240, v78, v79
	v_max3_f32 v239, v239, v77, v240
	v_mov_b32_e32 v240, v239
	s_nop 1
	v_permlane32_swap_b32_e32 v239, v240
	v_max_f32_e32 v239, v240, v239
	v_cmp_lt_f32_e32 vcc, s49, v239
	s_cmp_lg_u64 vcc, 0
	s_cselect_b64 s[0:1], -1, 0
	s_cbranch_vccnz .LBB0_561

.LBB0_567:
	v_max_f32_e32 v76, v49, v49
	v_max_f32_e32 v77, v48, v48
	v_max_f32_e32 v76, v77, v76
	s_nop 1
	v_max3_f32 v77, v50, v51, v33
	v_max3_f32 v76, v76, v32, v34
	v_max3_f32 v76, v76, v35, v52
	v_max3_f32 v77, v77, v54, v55
	v_max3_f32 v76, v76, v53, v36
	v_max3_f32 v77, v77, v38, v39
	v_max3_f32 v76, v76, v37, v56
	v_max3_f32 v77, v77, v58, v59
	v_max3_f32 v76, v76, v57, v40
	v_max3_f32 v77, v77, v42, v43
	v_max3_f32 v76, v76, v41, v60
	v_max3_f32 v77, v77, v62, v63
	v_max3_f32 v76, v76, v61, v44
	v_max3_f32 v77, v77, v46, v47
	v_max3_f32 v76, v76, v45, v77
	v_mov_b32_e32 v77, v76
	s_nop 1
	v_permlane32_swap_b32_e32 v76, v77
	v_max_f32_e32 v76, v77, v76
	v_cmp_lt_f32_e32 vcc, s49, v76
	s_cmp_lg_u64 vcc, 0
	v_add_f32_e32 v120, v235, v116
	s_cselect_b64 s[0:1], -1, 0
	s_cbranch_vccnz .LBB0_721

.LBB0_627:
	v_add_f32_e32 v197, v233, v68
	v_max_f32_e32 v68, v49, v48
	v_max3_f32 v69, v50, v51, v33
	v_max3_f32 v68, v68, v32, v34
	v_max3_f32 v68, v68, v35, v52
	v_max3_f32 v69, v69, v54, v55
	v_max3_f32 v68, v68, v53, v36
	v_max3_f32 v69, v69, v38, v39
	v_max3_f32 v68, v68, v37, v56
	v_max3_f32 v69, v69, v58, v59
	v_max3_f32 v68, v68, v57, v40
	v_max3_f32 v69, v69, v42, v43
	v_max3_f32 v68, v68, v41, v60
	v_max3_f32 v69, v69, v62, v63
	v_max3_f32 v68, v68, v61, v44
	v_max3_f32 v69, v69, v46, v47
	v_max3_f32 v68, v68, v45, v69
	v_mov_b32_e32 v69, v68
	s_nop 1
	v_permlane32_swap_b32_e32 v68, v69
	v_max_f32_e32 v68, v69, v68
	v_cmp_lt_f32_e32 vcc, s49, v68
	s_cmp_lg_u64 vcc, 0
	s_cselect_b64 s[50:51], -1, 0
	s_cbranch_vccnz .LBB0_637

.LBB0_632:
	v_add_f32_e32 v233, v197, v36
	v_max_f32_e32 v36, v81, v80
	v_max3_f32 v37, v82, v83, v65
	v_max3_f32 v36, v36, v64, v66
	v_max3_f32 v36, v36, v67, v84
	v_max3_f32 v37, v37, v86, v87
	v_max3_f32 v36, v36, v85, v68
	v_max3_f32 v37, v37, v70, v71
	v_max3_f32 v36, v36, v69, v88
	v_max3_f32 v37, v37, v90, v91
	v_max3_f32 v36, v36, v89, v72
	v_max3_f32 v37, v37, v74, v75
	v_max3_f32 v36, v36, v73, v92
	v_max3_f32 v37, v37, v94, v95
	v_max3_f32 v36, v36, v93, v76
	v_max3_f32 v37, v37, v78, v79
	v_max3_f32 v36, v36, v77, v37
	v_mov_b32_e32 v37, v36
	s_nop 1
	v_permlane32_swap_b32_e32 v36, v37
	v_max_f32_e32 v36, v37, v36
	v_cmp_lt_f32_e32 vcc, s49, v36
	s_cmp_lg_u64 vcc, 0
	s_cselect_b64 s[40:41], -1, 0
	s_cbranch_vccnz .LBB0_640

.LBB0_650:
	v_add_f32_e32 v233, v233, v68
	v_max_f32_e32 v68, v49, v48
	v_max3_f32 v69, v50, v51, v33
	v_max3_f32 v68, v68, v32, v34
	v_max3_f32 v68, v68, v35, v52
	v_max3_f32 v69, v69, v54, v55
	v_max3_f32 v68, v68, v53, v36
	v_max3_f32 v69, v69, v38, v39
	v_max3_f32 v68, v68, v37, v56
	v_max3_f32 v69, v69, v58, v59
	v_max3_f32 v68, v68, v57, v40
	v_max3_f32 v69, v69, v42, v43
	v_max3_f32 v68, v68, v41, v60
	v_max3_f32 v69, v69, v62, v63
	v_max3_f32 v68, v68, v61, v44
	v_max3_f32 v69, v69, v46, v47
	v_max3_f32 v68, v68, v45, v69
	v_mov_b32_e32 v69, v68
	s_nop 1
	v_permlane32_swap_b32_e32 v68, v69
	v_max_f32_e32 v68, v69, v68
	v_cmp_lt_f32_e32 vcc, s49, v68
	s_cmp_lg_u64 vcc, 0
	s_cselect_b64 s[66:67], -1, 0
	s_cbranch_vccnz .LBB0_704

.LBB0_661:
	v_add_f32_e32 v233, v233, v235
	v_max_f32_e32 v235, v81, v80
	v_max3_f32 v236, v82, v83, v65
	v_max3_f32 v235, v235, v64, v66
	v_max3_f32 v235, v235, v67, v84
	v_max3_f32 v236, v236, v86, v87
	v_max3_f32 v235, v235, v85, v68
	v_max3_f32 v236, v236, v70, v71
	v_max3_f32 v235, v235, v69, v88
	v_max3_f32 v236, v236, v90, v91
	v_max3_f32 v235, v235, v89, v72
	v_max3_f32 v236, v236, v74, v75
	v_max3_f32 v235, v235, v73, v92
	v_max3_f32 v236, v236, v94, v95
	v_max3_f32 v235, v235, v93, v76
	v_max3_f32 v236, v236, v78, v79
	v_max3_f32 v235, v235, v77, v236
	v_mov_b32_e32 v236, v235
	s_nop 1
	v_permlane32_swap_b32_e32 v235, v236
	v_max_f32_e32 v235, v236, v235
	v_cmp_lt_f32_e32 vcc, s49, v235
	s_cmp_lg_u64 vcc, 0
	s_cselect_b64 s[68:69], -1, 0
	s_cbranch_vccnz .LBB0_707

.LBB0_713:
	v_max_f32_e32 v76, v49, v49
	v_max_f32_e32 v77, v48, v48
	v_max_f32_e32 v76, v77, v76
	s_nop 1
	v_max3_f32 v77, v50, v51, v33
	v_max3_f32 v76, v76, v32, v34
	v_max3_f32 v76, v76, v35, v52
	v_max3_f32 v77, v77, v54, v55
	v_max3_f32 v76, v76, v53, v36
	v_max3_f32 v77, v77, v38, v39
	v_max3_f32 v76, v76, v37, v56
	v_max3_f32 v77, v77, v58, v59
	v_max3_f32 v76, v76, v57, v40
	v_max3_f32 v77, v77, v42, v43
	v_max3_f32 v76, v76, v41, v60
	v_max3_f32 v77, v77, v62, v63
	v_max3_f32 v76, v76, v61, v44
	v_max3_f32 v77, v77, v46, v47
	v_max3_f32 v76, v76, v45, v77
	v_mov_b32_e32 v77, v76
	s_nop 1
	v_permlane32_swap_b32_e32 v76, v77
	v_max_f32_e32 v76, v77, v76
	v_cmp_lt_f32_e32 vcc, s49, v76
	s_cmp_lg_u64 vcc, 0
	v_add_f32_e32 v116, v233, v116
	s_cselect_b64 s[0:1], -1, 0
	s_cbranch_vccnz .LBB0_724
